# K-loop head shortening in P7 and P1 (loop-edge edit): common K step takes one early-out instead of 3 test chains + 3 taken branches; rare prefetch blocks out of line
# speedup vs baseline: 1.0014x; 1.0014x over previous
.LBB0_331:
	s_cmp_lg_u32 s77, s10
	s_cselect_b64 s[60:61], -1, 0
	s_cbranch_scc1 .LBB0_330
	s_or_b64 s[2:3], s[4:5], s[60:61]
	s_or_b64 s[62:63], s[78:79], s[2:3]
	s_and_b64 vcc, exec, s[62:63]
	s_cbranch_vccnz .LBB0_333
	v_mov_b32_e32 v2, v204
	s_mov_b32 m0, s82
	v_ashrrev_i32_e32 v3, 31, v2
	v_lshl_add_u64 v[2:3], v[2:3], 2, s[0:1]
	global_load_lds_dwordx4 v[2:3], off

.LBB0_1210:
	s_cmp_eq_u32 s95, s65
	s_cbranch_scc1 .Lk7_slow
	s_cmp_eq_u32 s94, s65
	s_cbranch_scc1 .Lk7_slow
	s_mov_b64 s[6:7], 0
.LBB0_1216:
	s_add_i32 s65, s65, 2
	s_add_u32 s60, s78, 0x100
	v_add_u32_e32 v2, s97, v157
	s_addc_u32 s61, s79, 0
	ds_read_b128 v[186:189], v2
	ds_read_b128 v[190:193], v2 offset:1024
	ds_read_b128 v[194:197], v2 offset:2048
	ds_read_b128 v[198:201], v2 offset:3072
	v_add_u32_e32 v2, s8, v157
	s_and_b64 s[62:63], s[6:7], exec
	ds_read_b128 v[202:205], v2
	ds_read_b128 v[206:209], v2 offset:1024
	ds_read_b128 v[210:213], v2 offset:2048
	ds_read_b128 v[214:217], v2 offset:3072
	s_cselect_b32 s62, 0, s60
	s_cselect_b32 s63, 0, s61
	s_add_u32 s62, s48, s62
	s_addc_u32 s63, s49, s63
	s_add_u32 s71, s22, s78
	s_addc_u32 vcc_lo, s31, s79
	s_and_b64 s[80:81], s[6:7], exec
	s_cselect_b32 s81, s77, vcc_lo
	s_cselect_b32 s80, s76, s71
	v_cndmask_b32_e64 v2, v184, v156, s[6:7]
	v_cndmask_b32_e64 v166, v185, v158, s[6:7]
	v_cndmask_b32_e64 v5, v4, v177, s[6:7]
	v_cndmask_b32_e64 v151, v162, v178, s[6:7]
	v_lshl_add_u64 v[140:141], v[136:137], 0, s[78:79]
	s_add_i32 m0, s84, 0xc000
	ds_read_b128 v[218:221], v159
	ds_read_b128 v[222:225], v159 offset:1024
	ds_read_b128 v[226:229], v159 offset:2048
	ds_read_b128 v[230:233], v159 offset:3072
	ds_read_b128 v[234:237], v159 offset:4096
	ds_read_b128 v[238:241], v159 offset:5120
	ds_read_b128 v[242:245], v159 offset:6144
	ds_read_b128 v[246:249], v159 offset:7168
	global_load_lds_dwordx4 v[140:141], off
	v_lshl_add_u64 v[140:141], v[138:139], 0, s[78:79]
	s_add_i32 m0, s84, 0xe000
	s_nop 0
	global_load_lds_dwordx4 v[140:141], off
	s_waitcnt vmcnt(8)
	s_waitcnt lgkmcnt(0)
	s_barrier
	s_setprio 1
	s_waitcnt lgkmcnt(0)
	v_mfma_scale_f32_16x16x128_f8f6f4 v[130:133], v[186:193], v[218:225], v[130:133], v181, v182 op_sel_hi:[0,0,0]
	v_mfma_scale_f32_16x16x128_f8f6f4 v[126:129], v[194:201], v[218:225], v[126:129], v181, v182 op_sel_hi:[0,0,0]
	v_mfma_scale_f32_16x16x128_f8f6f4 v[122:125], v[186:193], v[226:233], v[122:125], v181, v182 op_sel_hi:[0,0,0]
	v_mfma_scale_f32_16x16x128_f8f6f4 v[118:121], v[194:201], v[226:233], v[118:121], v181, v182 op_sel_hi:[0,0,0]
	v_mfma_scale_f32_16x16x128_f8f6f4 v[114:117], v[186:193], v[234:241], v[114:117], v181, v182 op_sel_hi:[0,0,0]
	v_mfma_scale_f32_16x16x128_f8f6f4 v[110:113], v[194:201], v[234:241], v[110:113], v181, v182 op_sel_hi:[0,0,0]
	v_mfma_scale_f32_16x16x128_f8f6f4 v[106:109], v[186:193], v[242:249], v[106:109], v181, v182 op_sel_hi:[0,0,0]
	v_mfma_scale_f32_16x16x128_f8f6f4 v[102:105], v[194:201], v[242:249], v[102:105], v181, v182 op_sel_hi:[0,0,0]
	s_setprio 0
	s_setprio 1
	v_mfma_scale_f32_16x16x128_f8f6f4 v[98:101], v[202:209], v[218:225], v[98:101], v181, v182 op_sel_hi:[0,0,0]
	v_mfma_scale_f32_16x16x128_f8f6f4 v[94:97], v[210:217], v[218:225], v[94:97], v181, v182 op_sel_hi:[0,0,0]
	v_mfma_scale_f32_16x16x128_f8f6f4 v[90:93], v[202:209], v[226:233], v[90:93], v181, v182 op_sel_hi:[0,0,0]
	v_mfma_scale_f32_16x16x128_f8f6f4 v[86:89], v[210:217], v[226:233], v[86:89], v181, v182 op_sel_hi:[0,0,0]
	v_mfma_scale_f32_16x16x128_f8f6f4 v[82:85], v[202:209], v[234:241], v[82:85], v181, v182 op_sel_hi:[0,0,0]
	v_mfma_scale_f32_16x16x128_f8f6f4 v[78:81], v[210:217], v[234:241], v[78:81], v181, v182 op_sel_hi:[0,0,0]
	v_mfma_scale_f32_16x16x128_f8f6f4 v[74:77], v[202:209], v[242:249], v[74:77], v181, v182 op_sel_hi:[0,0,0]
	v_mfma_scale_f32_16x16x128_f8f6f4 v[70:73], v[210:217], v[242:249], v[70:73], v181, v182 op_sel_hi:[0,0,0]
	s_setprio 0
	s_barrier
	s_add_i32 s6, s97, s83
	v_lshl_add_u64 v[140:141], s[80:81], 0, v[148:149]
	s_mov_b32 m0, s6
	ds_read_b128 v[218:221], v159 offset:16384
	ds_read_b128 v[222:225], v159 offset:17408
	ds_read_b128 v[226:229], v159 offset:18432
	ds_read_b128 v[230:233], v159 offset:19456
	ds_read_b128 v[234:237], v159 offset:20480
	ds_read_b128 v[238:241], v159 offset:21504
	ds_read_b128 v[242:245], v159 offset:22528
	ds_read_b128 v[246:249], v159 offset:23552
	global_load_lds_dwordx4 v[140:141], off
	s_add_i32 m0, s6, 0x2000
	s_add_u32 s6, s80, s51
	v_lshl_add_u64 v[142:143], s[80:81], 0, v[160:161]
	s_addc_u32 s7, s81, 0
	s_add_i32 s71, s8, s83
	global_load_lds_dwordx4 v[142:143], off
	v_lshl_add_u64 v[144:145], s[6:7], 0, v[148:149]
	s_mov_b32 m0, s71
	v_lshl_add_u64 v[164:165], s[6:7], 0, v[160:161]
	global_load_lds_dwordx4 v[144:145], off
	s_add_i32 m0, s71, 0x2000
	v_mov_b32_e32 v167, v3
	global_load_lds_dwordx4 v[164:165], off
	s_mov_b32 m0, s84
	v_lshl_add_u64 v[168:169], s[62:63], 0, v[2:3]
	global_load_lds_dwordx4 v2, s[62:63]
	s_mov_b32 m0, s85
	s_nop 0
	global_load_lds_dwordx4 v166, s[62:63]
	s_waitcnt vmcnt(8)
	s_waitcnt lgkmcnt(0)
	v_lshl_add_u64 v[166:167], s[62:63], 0, v[166:167]
	s_barrier
	s_setprio 1
	s_waitcnt lgkmcnt(0)
	v_mfma_scale_f32_16x16x128_f8f6f4 v[66:69], v[186:193], v[218:225], v[66:69], v181, v182 op_sel_hi:[0,0,0]
	v_mfma_scale_f32_16x16x128_f8f6f4 v[62:65], v[194:201], v[218:225], v[62:65], v181, v182 op_sel_hi:[0,0,0]
	v_mfma_scale_f32_16x16x128_f8f6f4 v[58:61], v[186:193], v[226:233], v[58:61], v181, v182 op_sel_hi:[0,0,0]
	v_mfma_scale_f32_16x16x128_f8f6f4 v[54:57], v[194:201], v[226:233], v[54:57], v181, v182 op_sel_hi:[0,0,0]
	v_mfma_scale_f32_16x16x128_f8f6f4 v[50:53], v[186:193], v[234:241], v[50:53], v181, v182 op_sel_hi:[0,0,0]
	v_mfma_scale_f32_16x16x128_f8f6f4 v[46:49], v[194:201], v[234:241], v[46:49], v181, v182 op_sel_hi:[0,0,0]
	v_mfma_scale_f32_16x16x128_f8f6f4 v[42:45], v[186:193], v[242:249], v[42:45], v181, v182 op_sel_hi:[0,0,0]
	v_mfma_scale_f32_16x16x128_f8f6f4 v[38:41], v[194:201], v[242:249], v[38:41], v181, v182 op_sel_hi:[0,0,0]
	s_setprio 0
	s_setprio 1
	v_mfma_scale_f32_16x16x128_f8f6f4 v[34:37], v[202:209], v[218:225], v[34:37], v181, v182 op_sel_hi:[0,0,0]
	v_mfma_scale_f32_16x16x128_f8f6f4 v[30:33], v[210:217], v[218:225], v[30:33], v181, v182 op_sel_hi:[0,0,0]
	v_mfma_scale_f32_16x16x128_f8f6f4 v[26:29], v[202:209], v[226:233], v[26:29], v181, v182 op_sel_hi:[0,0,0]
	v_mfma_scale_f32_16x16x128_f8f6f4 v[22:25], v[210:217], v[226:233], v[22:25], v181, v182 op_sel_hi:[0,0,0]
	v_mfma_scale_f32_16x16x128_f8f6f4 v[18:21], v[202:209], v[234:241], v[18:21], v181, v182 op_sel_hi:[0,0,0]
	v_mfma_scale_f32_16x16x128_f8f6f4 v[14:17], v[210:217], v[234:241], v[14:17], v181, v182 op_sel_hi:[0,0,0]
	v_mfma_scale_f32_16x16x128_f8f6f4 v[10:13], v[202:209], v[242:249], v[10:13], v181, v182 op_sel_hi:[0,0,0]
	v_mfma_scale_f32_16x16x128_f8f6f4 v[6:9], v[210:217], v[242:249], v[6:9], v181, v182 op_sel_hi:[0,0,0]
	s_setprio 0
	s_barrier
	s_add_i32 s6, 0, 0x18000
	v_add_u32_e32 v2, s6, v157
	s_add_i32 s7, 0, 0x1c000
	ds_read_b128 v[186:189], v2
	ds_read_b128 v[190:193], v2 offset:1024
	ds_read_b128 v[194:197], v2 offset:2048
	ds_read_b128 v[198:201], v2 offset:3072
	v_add_u32_e32 v2, s7, v157
	ds_read_b128 v[202:205], v2
	ds_read_b128 v[206:209], v2 offset:1024
	ds_read_b128 v[210:213], v2 offset:2048
	ds_read_b128 v[214:217], v2 offset:3072
	s_mov_b32 m0, s86
	ds_read_b128 v[218:221], v159 offset:32768
	ds_read_b128 v[222:225], v159 offset:33792
	ds_read_b128 v[226:229], v159 offset:34816
	ds_read_b128 v[230:233], v159 offset:35840
	ds_read_b128 v[234:237], v159 offset:36864
	ds_read_b128 v[238:241], v159 offset:37888
	ds_read_b128 v[242:245], v159 offset:38912
	ds_read_b128 v[246:249], v159 offset:39936
	global_load_lds_dwordx4 v5, s[62:63]
	s_mov_b32 m0, s87
	s_nop 0
	global_load_lds_dwordx4 v151, s[62:63]
	s_waitcnt vmcnt(8)
	s_waitcnt lgkmcnt(0)
	s_barrier
	s_setprio 1
	s_waitcnt lgkmcnt(0)
	v_mfma_scale_f32_16x16x128_f8f6f4 v[130:133], v[186:193], v[218:225], v[130:133], v181, v182 op_sel_hi:[0,0,0]
	v_mfma_scale_f32_16x16x128_f8f6f4 v[126:129], v[194:201], v[218:225], v[126:129], v181, v182 op_sel_hi:[0,0,0]
	v_mfma_scale_f32_16x16x128_f8f6f4 v[122:125], v[186:193], v[226:233], v[122:125], v181, v182 op_sel_hi:[0,0,0]
	v_mfma_scale_f32_16x16x128_f8f6f4 v[118:121], v[194:201], v[226:233], v[118:121], v181, v182 op_sel_hi:[0,0,0]
	v_mfma_scale_f32_16x16x128_f8f6f4 v[114:117], v[186:193], v[234:241], v[114:117], v181, v182 op_sel_hi:[0,0,0]
	v_mfma_scale_f32_16x16x128_f8f6f4 v[110:113], v[194:201], v[234:241], v[110:113], v181, v182 op_sel_hi:[0,0,0]
	v_mfma_scale_f32_16x16x128_f8f6f4 v[106:109], v[186:193], v[242:249], v[106:109], v181, v182 op_sel_hi:[0,0,0]
	v_mfma_scale_f32_16x16x128_f8f6f4 v[102:105], v[194:201], v[242:249], v[102:105], v181, v182 op_sel_hi:[0,0,0]
	s_setprio 0
	s_setprio 1
	v_mfma_scale_f32_16x16x128_f8f6f4 v[98:101], v[202:209], v[218:225], v[98:101], v181, v182 op_sel_hi:[0,0,0]
	v_mfma_scale_f32_16x16x128_f8f6f4 v[94:97], v[210:217], v[218:225], v[94:97], v181, v182 op_sel_hi:[0,0,0]
	v_mfma_scale_f32_16x16x128_f8f6f4 v[90:93], v[202:209], v[226:233], v[90:93], v181, v182 op_sel_hi:[0,0,0]
	v_mfma_scale_f32_16x16x128_f8f6f4 v[86:89], v[210:217], v[226:233], v[86:89], v181, v182 op_sel_hi:[0,0,0]
	v_mfma_scale_f32_16x16x128_f8f6f4 v[82:85], v[202:209], v[234:241], v[82:85], v181, v182 op_sel_hi:[0,0,0]
	v_mfma_scale_f32_16x16x128_f8f6f4 v[78:81], v[210:217], v[234:241], v[78:81], v181, v182 op_sel_hi:[0,0,0]
	v_mfma_scale_f32_16x16x128_f8f6f4 v[74:77], v[202:209], v[242:249], v[74:77], v181, v182 op_sel_hi:[0,0,0]
	v_mfma_scale_f32_16x16x128_f8f6f4 v[70:73], v[210:217], v[242:249], v[70:73], v181, v182 op_sel_hi:[0,0,0]
	s_setprio 0
	s_barrier
	s_add_i32 s6, s6, s83
	v_lshl_add_u64 v[140:141], v[140:141], 0, s[38:39]
	s_mov_b32 m0, s6
	ds_read_b128 v[218:221], v159 offset:49152
	ds_read_b128 v[222:225], v159 offset:50176
	ds_read_b128 v[226:229], v159 offset:51200
	ds_read_b128 v[230:233], v159 offset:52224
	ds_read_b128 v[234:237], v159 offset:53248
	ds_read_b128 v[238:241], v159 offset:54272
	ds_read_b128 v[242:245], v159 offset:55296
	ds_read_b128 v[246:249], v159 offset:56320
	global_load_lds_dwordx4 v[140:141], off
	v_lshl_add_u64 v[140:141], v[142:143], 0, s[38:39]
	s_add_i32 m0, s6, 0x2000
	s_add_i32 s6, s7, s83
	global_load_lds_dwordx4 v[140:141], off
	v_lshl_add_u64 v[140:141], v[144:145], 0, s[38:39]
	s_mov_b32 m0, s6
	s_nop 0
	global_load_lds_dwordx4 v[140:141], off
	v_lshl_add_u64 v[140:141], v[164:165], 0, s[38:39]
	s_add_i32 m0, s6, 0x2000
	s_nop 0
	global_load_lds_dwordx4 v[140:141], off
	v_lshl_add_u64 v[140:141], v[168:169], 0, s[38:39]
	s_mov_b32 m0, s90
	s_nop 0
	global_load_lds_dwordx4 v[140:141], off
	v_lshl_add_u64 v[140:141], v[166:167], 0, s[38:39]
	s_mov_b32 m0, s91
	s_nop 0
	global_load_lds_dwordx4 v[140:141], off
	s_waitcnt vmcnt(8)
	s_waitcnt lgkmcnt(0)
	s_barrier
	s_setprio 1
	s_waitcnt lgkmcnt(0)
	v_mfma_scale_f32_16x16x128_f8f6f4 v[66:69], v[186:193], v[218:225], v[66:69], v181, v182 op_sel_hi:[0,0,0]
	v_mfma_scale_f32_16x16x128_f8f6f4 v[62:65], v[194:201], v[218:225], v[62:65], v181, v182 op_sel_hi:[0,0,0]
	v_mfma_scale_f32_16x16x128_f8f6f4 v[58:61], v[186:193], v[226:233], v[58:61], v181, v182 op_sel_hi:[0,0,0]
	v_mfma_scale_f32_16x16x128_f8f6f4 v[54:57], v[194:201], v[226:233], v[54:57], v181, v182 op_sel_hi:[0,0,0]
	v_mfma_scale_f32_16x16x128_f8f6f4 v[50:53], v[186:193], v[234:241], v[50:53], v181, v182 op_sel_hi:[0,0,0]
	v_mfma_scale_f32_16x16x128_f8f6f4 v[46:49], v[194:201], v[234:241], v[46:49], v181, v182 op_sel_hi:[0,0,0]
	v_mfma_scale_f32_16x16x128_f8f6f4 v[42:45], v[186:193], v[242:249], v[42:45], v181, v182 op_sel_hi:[0,0,0]
	v_mfma_scale_f32_16x16x128_f8f6f4 v[38:41], v[194:201], v[242:249], v[38:41], v181, v182 op_sel_hi:[0,0,0]
	s_setprio 0
	s_setprio 1
	v_mfma_scale_f32_16x16x128_f8f6f4 v[34:37], v[202:209], v[218:225], v[34:37], v181, v182 op_sel_hi:[0,0,0]
	v_mfma_scale_f32_16x16x128_f8f6f4 v[30:33], v[210:217], v[218:225], v[30:33], v181, v182 op_sel_hi:[0,0,0]
	v_mfma_scale_f32_16x16x128_f8f6f4 v[26:29], v[202:209], v[226:233], v[26:29], v181, v182 op_sel_hi:[0,0,0]
	v_mfma_scale_f32_16x16x128_f8f6f4 v[22:25], v[210:217], v[226:233], v[22:25], v181, v182 op_sel_hi:[0,0,0]
	v_mfma_scale_f32_16x16x128_f8f6f4 v[18:21], v[202:209], v[234:241], v[18:21], v181, v182 op_sel_hi:[0,0,0]
	v_mfma_scale_f32_16x16x128_f8f6f4 v[14:17], v[210:217], v[234:241], v[14:17], v181, v182 op_sel_hi:[0,0,0]
	v_mfma_scale_f32_16x16x128_f8f6f4 v[10:13], v[202:209], v[242:249], v[10:13], v181, v182 op_sel_hi:[0,0,0]
	v_mfma_scale_f32_16x16x128_f8f6f4 v[6:9], v[210:217], v[242:249], v[6:9], v181, v182 op_sel_hi:[0,0,0]
	s_setprio 0
	s_barrier
	s_cmp_ge_i32 s65, s15
	s_cbranch_scc1 .LBB0_1218
	s_mov_b64 s[78:79], s[60:61]
	s_branch .LBB0_1210
.Lk7_slow:
	s_cmp_eq_u32 s95, s65
	s_cselect_b64 s[6:7], -1, 0
	s_and_b64 s[60:61], s[74:75], s[6:7]
	s_and_b64 s[62:63], s[16:17], s[60:61]
	s_andn2_b64 vcc, exec, s[62:63]
	s_cbranch_vccnz .LBB0_1212
	s_add_i32 s62, s30, 0
	s_add_i32 m0, s62, 0x21000
	s_nop 0
	global_load_lds_dwordx4 v[134:135], off

.LBB0_1214:
	s_andn2_b64 vcc, exec, s[60:61]
	s_cbranch_vccnz .LBB0_1216
	ds_read2st64_b32 v[140:141], v170 offset1:2
	ds_read2st64_b32 v[142:143], v171 offset1:2
	s_waitcnt lgkmcnt(0)
	v_min_u32_e32 v2, 0x3fff, v140
	v_mad_u64_u32 v[144:145], s[60:61], v2, s14, v[152:153]
	v_min_u32_e32 v2, 0x3fff, v141
	v_min_u32_e32 v5, 0x3fff, v142
	v_mad_u64_u32 v[140:141], s[60:61], v2, s14, v[152:153]
	v_min_u32_e32 v2, 0x3fff, v143
	v_lshl_add_u32 v156, v144, 1, v176
	v_mad_u64_u32 v[144:145], s[60:61], v5, s14, v[154:155]
	v_lshl_add_u32 v177, v140, 1, v176
	v_mad_u64_u32 v[140:141], s[60:61], v2, s14, v[154:155]
	v_lshl_add_u32 v158, v144, 1, v176
	v_lshl_add_u32 v178, v140, 1, v176
	s_branch .LBB0_1216
